# batch3: + P8 second token row loads issued with the first row's
# baseline (speedup 1.0000x reference)
.LBB0_826:
	v_mov_b64_e32 v[34:35], v[46:47]
	s_barrier
	s_add_i32 s10, s34, s36
	global_load_dword v93, v[34:35], off
	global_load_dword v81, v[34:35], off offset:64
	global_load_dword v94, v[34:35], off offset:512
	global_load_dword v82, v[34:35], off offset:576
	global_load_dword v95, v[34:35], off offset:1024
	global_load_dword v83, v[34:35], off offset:1088
	global_load_dword v96, v[34:35], off offset:1536
	global_load_dword v84, v[34:35], off offset:1600
	global_load_dword v97, v[34:35], off offset:2048
	global_load_dword v85, v[34:35], off offset:2112
	global_load_dword v98, v[34:35], off offset:2560
	global_load_dword v87, v[34:35], off offset:2624
	global_load_dword v99, v[34:35], off offset:3072
	global_load_dword v88, v[34:35], off offset:3136
	global_load_dword v100, v[34:35], off offset:3584
	global_load_dword v89, v[34:35], off offset:3648
	v_add_co_u32_e32 v34, vcc, s33, v34
	s_ashr_i32 s11, s10, 31
	s_nop 0
	v_addc_co_u32_e32 v35, vcc, 0, v35, vcc
	s_lshl_b64 s[12:13], s[10:11], 12
	global_load_dword v101, v[34:35], off
	global_load_dword v91, v[34:35], off offset:64
	global_load_dword v102, v[34:35], off offset:512
	global_load_dword v92, v[34:35], off offset:576
	global_load_dword v103, v[34:35], off offset:1024
	global_load_dword v90, v[34:35], off offset:1088
	global_load_dword v104, v[34:35], off offset:1536
	global_load_dword v86, v[34:35], off offset:1600
	global_load_dword v105, v[34:35], off offset:2048
	global_load_dword v80, v[34:35], off offset:2112
	global_load_dword v106, v[34:35], off offset:2560
	global_load_dword v79, v[34:35], off offset:2624
	global_load_dword v107, v[34:35], off offset:3072
	global_load_dword v78, v[34:35], off offset:3136
	global_load_dword v108, v[34:35], off offset:3584
	global_load_dword v77, v[34:35], off offset:3648
	v_lshl_add_u64 v[34:35], v[56:57], 0, s[12:13]
	global_load_dwordx2 v[36:37], v[34:35], off
	global_load_dwordx2 v[38:39], v[34:35], off offset:512
	global_load_dwordx2 v[40:41], v[34:35], off offset:1024
	global_load_dwordx2 v[42:43], v[34:35], off offset:1536
	global_load_dwordx2 v[44:45], v[34:35], off offset:2048
	global_load_dwordx2 v[74:75], v[34:35], off offset:2560
	global_load_dwordx2 v[110:111], v[34:35], off offset:3072
	s_waitcnt lgkmcnt(0)
	v_and_b32_e32 v61, 64, v71
	global_load_dwordx2 v[34:35], v[34:35], off offset:3584
	v_xor_b32_e32 v73, 1, v71
	v_add_u32_e32 v109, 64, v61
	v_cmp_lt_i32_e32 vcc, v73, v109
	s_lshl_b64 s[12:13], s[10:11], 11
	v_lshl_add_u64 v[142:143], v[58:59], 0, s[12:13]
	v_cndmask_b32_e32 v61, v71, v73, vcc
	v_lshlrev_b32_e32 v61, 2, v61
	s_add_i32 s10, s10, 1
	s_ashr_i32 s11, s10, 31
	s_lshl_b64 s[12:13], s[10:11], 12
	s_lshl_b64 s[10:11], s[10:11], 11
	v_lshl_add_u64 v[190:191], v[56:57], 0, s[12:13]
	global_load_dwordx2 v[174:175], v[190:191], off
	global_load_dwordx2 v[176:177], v[190:191], off offset:512
	global_load_dwordx2 v[178:179], v[190:191], off offset:1024
	global_load_dwordx2 v[180:181], v[190:191], off offset:1536
	global_load_dwordx2 v[182:183], v[190:191], off offset:2048
	global_load_dwordx2 v[184:185], v[190:191], off offset:2560
	global_load_dwordx2 v[186:187], v[190:191], off offset:3072
	global_load_dwordx2 v[188:189], v[190:191], off offset:3584
	s_waitcnt vmcnt(15)
	v_lshlrev_b32_e32 v112, 16, v36
	v_and_b32_e32 v113, 0xffff0000, v36
	v_lshlrev_b32_e32 v36, 16, v37
	v_and_b32_e32 v37, 0xffff0000, v37
	s_waitcnt vmcnt(14)
	v_and_b32_e32 v115, 0xffff0000, v38
	v_and_b32_e32 v117, 0xffff0000, v39
	v_lshlrev_b32_e32 v114, 16, v38
	v_lshlrev_b32_e32 v116, 16, v39
	s_waitcnt vmcnt(13)
	v_lshlrev_b32_e32 v118, 16, v40
	v_and_b32_e32 v119, 0xffff0000, v40
	v_lshlrev_b32_e32 v120, 16, v41
	v_and_b32_e32 v121, 0xffff0000, v41
	v_mov_b32_e32 v40, v113
	v_mov_b32_e32 v41, v115
	v_mov_b32_e32 v124, v37
	v_mov_b32_e32 v125, v117
	v_mov_b32_e32 v38, v112
	v_mov_b32_e32 v39, v114
	v_mov_b32_e32 v122, v36
	v_mov_b32_e32 v123, v116
	v_pk_mul_f32 v[40:41], v[40:41], v[40:41]
	v_pk_mul_f32 v[124:125], v[124:125], v[124:125]
	v_mov_b32_e32 v128, v119
	v_mov_b32_e32 v129, v121
	v_pk_fma_f32 v[38:39], v[38:39], v[38:39], v[40:41]
	v_pk_fma_f32 v[40:41], v[122:123], v[122:123], v[124:125]
	v_mov_b32_e32 v126, v118
	v_mov_b32_e32 v127, v120
	v_pk_add_f32 v[38:39], v[38:39], v[40:41]
	v_pk_mul_f32 v[40:41], v[128:129], v[128:129]
	s_waitcnt vmcnt(12)
	v_and_b32_e32 v123, 0xffff0000, v42
	v_pk_fma_f32 v[40:41], v[126:127], v[126:127], v[40:41]
	v_lshlrev_b32_e32 v122, 16, v42
	v_mul_f32_e32 v42, v123, v123
	v_and_b32_e32 v127, 0xffff0000, v43
	v_pk_fma_f32 v[124:125], v[122:123], v[122:123], v[42:43] op_sel_hi:[1,1,0]
	v_lshlrev_b32_e32 v126, 16, v43
	v_mul_f32_e32 v42, v127, v127
	s_waitcnt vmcnt(11)
	v_lshlrev_b32_e32 v128, 16, v44
	v_and_b32_e32 v129, 0xffff0000, v44
	v_lshlrev_b32_e32 v132, 16, v45
	v_and_b32_e32 v133, 0xffff0000, v45
	v_pk_add_f32 v[38:39], v[38:39], v[38:39] op_sel:[0,1] op_sel_hi:[1,0]
	v_pk_add_f32 v[40:41], v[40:41], v[40:41] op_sel:[0,1] op_sel_hi:[1,0]
	v_pk_fma_f32 v[42:43], v[126:127], v[126:127], v[42:43] op_sel_hi:[1,1,0]
	v_pk_mul_f32 v[130:131], v[128:129], v[128:129]
	v_pk_mul_f32 v[44:45], v[132:133], v[132:133]
	v_mov_b32_e32 v39, v130
	v_mov_b32_e32 v41, v131
	v_mov_b32_e32 v125, v44
	v_mov_b32_e32 v43, v45
	v_pk_add_f32 v[38:39], v[38:39], v[40:41]
	v_pk_add_f32 v[40:41], v[124:125], v[42:43]
	s_waitcnt vmcnt(10)
	v_and_b32_e32 v125, 0xffff0000, v74
	v_and_b32_e32 v131, 0xffff0000, v75
	v_lshlrev_b32_e32 v124, 16, v74
	v_lshlrev_b32_e32 v130, 16, v75
	v_mov_b32_e32 v42, v125
	v_mov_b32_e32 v43, v131
	v_pk_add_f32 v[38:39], v[38:39], v[40:41]
	v_mov_b32_e32 v40, v124
	v_mov_b32_e32 v41, v130
	v_pk_mul_f32 v[42:43], v[42:43], v[42:43]
	s_waitcnt vmcnt(9)
	v_and_b32_e32 v135, 0xffff0000, v110
	v_and_b32_e32 v137, 0xffff0000, v111
	v_pk_fma_f32 v[40:41], v[40:41], v[40:41], v[42:43]
	v_lshlrev_b32_e32 v134, 16, v110
	v_mul_f32_e32 v42, v135, v135
	v_lshlrev_b32_e32 v136, 16, v111
	v_mul_f32_e32 v44, v137, v137
	s_waitcnt vmcnt(8)
	v_lshlrev_b32_e32 v138, 16, v34
	v_and_b32_e32 v139, 0xffff0000, v34
	v_lshlrev_b32_e32 v140, 16, v35
	v_and_b32_e32 v141, 0xffff0000, v35
	v_pk_add_f32 v[38:39], v[38:39], v[38:39] op_sel:[0,1] op_sel_hi:[1,0]
	v_pk_add_f32 v[40:41], v[40:41], v[40:41] op_sel:[0,1] op_sel_hi:[1,0]
	v_pk_fma_f32 v[42:43], v[134:135], v[134:135], v[42:43] op_sel_hi:[1,1,0]
	v_pk_fma_f32 v[44:45], v[136:137], v[136:137], v[44:45] op_sel_hi:[1,1,0]
	v_pk_mul_f32 v[74:75], v[138:139], v[138:139]
	v_pk_mul_f32 v[34:35], v[140:141], v[140:141]
	v_mov_b32_e32 v39, v74
	v_mov_b32_e32 v41, v75
	v_mov_b32_e32 v43, v34
	v_mov_b32_e32 v45, v35
	v_pk_add_f32 v[38:39], v[38:39], v[40:41]
	v_pk_add_f32 v[34:35], v[42:43], v[44:45]
	s_nop 0
	v_pk_add_f32 v[34:35], v[38:39], v[34:35]
	v_xor_b32_e32 v38, 2, v71
	v_add_f32_e32 v34, v34, v35
	ds_bpermute_b32 v35, v61, v34
	v_cmp_lt_i32_e32 vcc, v38, v109
	s_waitcnt lgkmcnt(0)
	v_add_f32_e32 v34, v34, v35
	v_cndmask_b32_e32 v38, v71, v38, vcc
	v_lshlrev_b32_e32 v73, 2, v38
	ds_bpermute_b32 v35, v73, v34
	v_xor_b32_e32 v38, 4, v71
	v_cmp_lt_i32_e32 vcc, v38, v109
	s_waitcnt lgkmcnt(0)
	v_add_f32_e32 v34, v34, v35
	v_cndmask_b32_e32 v38, v71, v38, vcc
	v_lshlrev_b32_e32 v74, 2, v38
	ds_bpermute_b32 v35, v74, v34
	v_xor_b32_e32 v38, 8, v71
	v_cmp_lt_i32_e32 vcc, v38, v109
	s_waitcnt lgkmcnt(0)
	v_add_f32_e32 v34, v34, v35
	v_cndmask_b32_e32 v38, v71, v38, vcc
	v_lshlrev_b32_e32 v75, 2, v38
	ds_bpermute_b32 v35, v75, v34
	v_xor_b32_e32 v38, 16, v71
	v_cmp_lt_i32_e32 vcc, v38, v109
	s_waitcnt lgkmcnt(0)
	v_add_f32_e32 v34, v34, v35
	v_cndmask_b32_e32 v38, v71, v38, vcc
	v_lshlrev_b32_e32 v76, 2, v38
	ds_bpermute_b32 v35, v76, v34
	v_xor_b32_e32 v38, 32, v71
	v_cmp_lt_i32_e32 vcc, v38, v109
	s_waitcnt lgkmcnt(0)
	v_add_f32_e32 v34, v34, v35
	v_cndmask_b32_e32 v38, v71, v38, vcc
	v_lshlrev_b32_e32 v109, 2, v38
	ds_bpermute_b32 v35, v109, v34
	s_waitcnt lgkmcnt(0)
	v_add_f32_e32 v34, v34, v35
	v_fmamk_f32 v34, v34, 0x3a000000, v67
	v_mul_f32_e32 v35, 0x4b800000, v34
	v_cmp_gt_f32_e32 vcc, s38, v34
	s_nop 1
	v_cndmask_b32_e32 v34, v34, v35, vcc
	v_rsq_f32_e32 v34, v34
	s_nop 0
	v_mul_f32_e32 v35, 0x45800000, v34
	v_cndmask_b32_e32 v144, v34, v35, vcc
	v_pk_mul_f32 v[34:35], v[144:145], v[112:113] op_sel_hi:[0,1]
	v_pk_mul_f32 v[34:35], v[30:31], v[34:35]
	v_pk_mul_f32 v[36:37], v[144:145], v[36:37] op_sel_hi:[0,1]
	v_mov_b32_e32 v145, 0
	v_cvt_pk_fp8_f32 v145, v34, v35
	v_pk_mul_f32 v[36:37], v[32:33], v[36:37]
	v_pk_mul_f32 v[38:39], v[144:145], v[114:115] op_sel_hi:[0,1]
	v_cvt_pk_fp8_f32 v145, v36, v37 op_sel:[0,0,1]
	v_pk_mul_f32 v[38:39], v[26:27], v[38:39]
	v_mov_b32_e32 v114, 0
	v_cvt_pk_fp8_f32 v114, v38, v39
	v_pk_mul_f32 v[42:43], v[144:145], v[118:119] op_sel_hi:[0,1]
	v_pk_mul_f32 v[42:43], v[22:23], v[42:43]
	v_mov_b32_e32 v115, 0
	v_pk_mul_f32 v[110:111], v[144:145], v[122:123] op_sel_hi:[0,1]
	v_pk_mul_f32 v[40:41], v[144:145], v[116:117] op_sel_hi:[0,1]
	v_cvt_pk_fp8_f32 v115, v42, v43
	v_pk_mul_f32 v[110:111], v[18:19], v[110:111]
	v_mov_b32_e32 v116, 0
	v_cvt_pk_fp8_f32 v116, v110, v111
	v_pk_mul_f32 v[40:41], v[28:29], v[40:41]
	v_pk_mul_f32 v[44:45], v[144:145], v[120:121] op_sel_hi:[0,1]
	v_cvt_pk_fp8_f32 v114, v40, v41 op_sel:[0,0,1]
	v_pk_mul_f32 v[44:45], v[24:25], v[44:45]
	v_pk_mul_f32 v[112:113], v[144:145], v[126:127] op_sel_hi:[0,1]
	v_cvt_pk_fp8_f32 v115, v44, v45 op_sel:[0,0,1]
	v_pk_mul_f32 v[112:113], v[20:21], v[112:113]
	v_pk_mul_f32 v[118:119], v[144:145], v[124:125] op_sel_hi:[0,1]
	v_cvt_pk_fp8_f32 v116, v112, v113 op_sel:[0,0,1]
	global_store_dword v[142:143], v145, off
	global_store_dword v[142:143], v114, off offset:256
	global_store_dword v[142:143], v115, off offset:512
	global_store_dword v[142:143], v116, off offset:768
	v_pk_mul_f32 v[114:115], v[144:145], v[128:129] op_sel_hi:[0,1]
	v_pk_mul_f32 v[114:115], v[14:15], v[114:115]
	v_pk_mul_f32 v[116:117], v[144:145], v[132:133] op_sel_hi:[0,1]
	v_mov_b32_e32 v132, 0
	v_cvt_pk_fp8_f32 v132, v114, v115
	v_pk_mul_f32 v[118:119], v[10:11], v[118:119]
	v_mov_b32_e32 v133, 0
	v_pk_mul_f32 v[122:123], v[144:145], v[134:135] op_sel_hi:[0,1]
	v_cvt_pk_fp8_f32 v133, v118, v119
	v_pk_mul_f32 v[120:121], v[144:145], v[130:131] op_sel_hi:[0,1]
	v_pk_mul_f32 v[122:123], v[6:7], v[122:123]
	v_mov_b32_e32 v130, 0
	v_pk_mul_f32 v[126:127], v[144:145], v[138:139] op_sel_hi:[0,1]
	v_cvt_pk_fp8_f32 v130, v122, v123
	v_pk_mul_f32 v[126:127], v[2:3], v[126:127]
	v_mov_b32_e32 v131, 0
	v_pk_mul_f32 v[116:117], v[16:17], v[116:117]
	v_cvt_pk_fp8_f32 v131, v126, v127
	v_cvt_pk_fp8_f32 v132, v116, v117 op_sel:[0,0,1]
	v_pk_mul_f32 v[120:121], v[12:13], v[120:121]
	v_pk_mul_f32 v[124:125], v[144:145], v[136:137] op_sel_hi:[0,1]
	v_cvt_pk_fp8_f32 v133, v120, v121 op_sel:[0,0,1]
	v_pk_mul_f32 v[124:125], v[8:9], v[124:125]
	v_pk_mul_f32 v[128:129], v[144:145], v[140:141] op_sel_hi:[0,1]
	v_cvt_pk_fp8_f32 v130, v124, v125 op_sel:[0,0,1]
	v_pk_mul_f32 v[128:129], v[4:5], v[128:129]
	s_nop 0
	v_cvt_pk_fp8_f32 v131, v128, v129 op_sel:[0,0,1]
	global_store_dword v[142:143], v132, off offset:1024
	global_store_dword v[142:143], v133, off offset:1280
	global_store_dword v[142:143], v130, off offset:1536
	global_store_dword v[142:143], v131, off offset:1792
	s_waitcnt vmcnt(8)
	v_mov_b64_e32 v[132:133], v[174:175]
	v_mov_b64_e32 v[134:135], v[176:177]
	v_mov_b64_e32 v[136:137], v[178:179]
	v_mov_b64_e32 v[138:139], v[180:181]
	v_mov_b64_e32 v[140:141], v[182:183]
	v_mov_b64_e32 v[142:143], v[184:185]
	v_mov_b64_e32 v[144:145], v[186:187]
	v_mov_b64_e32 v[130:131], v[188:189]
	ds_write_b128 v62, v[34:37]
	ds_write_b128 v62, v[38:41] offset:1024
	ds_write_b128 v62, v[42:45] offset:2048
	ds_write_b128 v62, v[110:113] offset:3072
	ds_write_b128 v62, v[114:117] offset:4096
	ds_write_b128 v62, v[118:121] offset:5120
	ds_write_b128 v62, v[122:125] offset:6144
	ds_write_b128 v62, v[126:129] offset:7168
	v_lshl_add_u64 v[44:45], v[58:59], 0, s[10:11]
	s_waitcnt vmcnt(8)
	v_and_b32_e32 v147, 0xffff0000, v132
	s_waitcnt vmcnt(8)
	v_and_b32_e32 v149, 0xffff0000, v134
	v_lshlrev_b32_e32 v146, 16, v132
	v_lshlrev_b32_e32 v132, 16, v133
	v_and_b32_e32 v133, 0xffff0000, v133
	v_lshlrev_b32_e32 v148, 16, v134
	v_lshlrev_b32_e32 v134, 16, v135
	v_and_b32_e32 v135, 0xffff0000, v135
	v_mov_b32_e32 v152, v147
	v_mov_b32_e32 v153, v149
	v_mov_b32_e32 v150, v146
	v_mov_b32_e32 v151, v148
	v_pk_mul_f32 v[152:153], v[152:153], v[152:153]
	v_mov_b32_e32 v154, v133
	v_mov_b32_e32 v155, v135
	v_pk_fma_f32 v[150:151], v[150:151], v[150:151], v[152:153]
	v_mov_b32_e32 v152, v132
	v_mov_b32_e32 v153, v134
	v_pk_mul_f32 v[154:155], v[154:155], v[154:155]
	s_waitcnt vmcnt(8)
	v_lshlrev_b32_e32 v162, 16, v140
	v_pk_fma_f32 v[152:153], v[152:153], v[152:153], v[154:155]
	v_and_b32_e32 v163, 0xffff0000, v140
	v_pk_add_f32 v[150:151], v[150:151], v[152:153]
	v_lshlrev_b32_e32 v152, 16, v136
	v_and_b32_e32 v153, 0xffff0000, v136
	v_lshlrev_b32_e32 v136, 16, v137
	v_and_b32_e32 v137, 0xffff0000, v137
	v_mov_b32_e32 v156, v153
	v_mov_b32_e32 v157, v137
	v_mov_b32_e32 v154, v152
	v_mov_b32_e32 v155, v136
	v_pk_mul_f32 v[156:157], v[156:157], v[156:157]
	v_lshlrev_b32_e32 v140, 16, v141
	v_pk_fma_f32 v[154:155], v[154:155], v[154:155], v[156:157]
	v_and_b32_e32 v157, 0xffff0000, v138
	v_lshlrev_b32_e32 v156, 16, v138
	v_mul_f32_e32 v138, v157, v157
	v_pk_fma_f32 v[158:159], v[156:157], v[156:157], v[138:139] op_sel_hi:[1,1,0]
	v_lshlrev_b32_e32 v138, 16, v139
	v_and_b32_e32 v139, 0xffff0000, v139
	v_mul_f32_e32 v160, v139, v139
	v_and_b32_e32 v141, 0xffff0000, v141
	v_pk_add_f32 v[150:151], v[150:151], v[150:151] op_sel:[0,1] op_sel_hi:[1,0]
	v_pk_add_f32 v[154:155], v[154:155], v[154:155] op_sel:[0,1] op_sel_hi:[1,0]
	v_pk_fma_f32 v[160:161], v[138:139], v[138:139], v[160:161] op_sel_hi:[1,1,0]
	v_pk_mul_f32 v[164:165], v[162:163], v[162:163]
	v_pk_mul_f32 v[166:167], v[140:141], v[140:141]
	v_mov_b32_e32 v151, v164
	v_mov_b32_e32 v155, v165
	v_mov_b32_e32 v159, v166
	v_mov_b32_e32 v161, v167
	v_pk_add_f32 v[150:151], v[150:151], v[154:155]
	v_pk_add_f32 v[154:155], v[158:159], v[160:161]
	s_waitcnt vmcnt(8)
	v_lshlrev_b32_e32 v168, 16, v130
	v_pk_add_f32 v[150:151], v[150:151], v[154:155]
	v_lshlrev_b32_e32 v154, 16, v142
	v_and_b32_e32 v155, 0xffff0000, v142
	v_lshlrev_b32_e32 v142, 16, v143
	v_and_b32_e32 v143, 0xffff0000, v143
	v_mov_b32_e32 v160, v155
	v_mov_b32_e32 v161, v143
	v_mov_b32_e32 v158, v154
	v_mov_b32_e32 v159, v142
	v_pk_mul_f32 v[160:161], v[160:161], v[160:161]
	v_and_b32_e32 v169, 0xffff0000, v130
	v_pk_fma_f32 v[158:159], v[158:159], v[158:159], v[160:161]
	v_and_b32_e32 v161, 0xffff0000, v144
	v_lshlrev_b32_e32 v160, 16, v144
	v_mul_f32_e32 v144, v161, v161
	v_pk_fma_f32 v[164:165], v[160:161], v[160:161], v[144:145] op_sel_hi:[1,1,0]
	v_lshlrev_b32_e32 v144, 16, v145
	v_and_b32_e32 v145, 0xffff0000, v145
	v_mul_f32_e32 v166, v145, v145
	v_lshlrev_b32_e32 v130, 16, v131
	v_and_b32_e32 v131, 0xffff0000, v131
	v_pk_add_f32 v[150:151], v[150:151], v[150:151] op_sel:[0,1] op_sel_hi:[1,0]
	v_pk_add_f32 v[158:159], v[158:159], v[158:159] op_sel:[0,1] op_sel_hi:[1,0]
	v_pk_fma_f32 v[166:167], v[144:145], v[144:145], v[166:167] op_sel_hi:[1,1,0]
	v_pk_mul_f32 v[170:171], v[168:169], v[168:169]
	v_pk_mul_f32 v[172:173], v[130:131], v[130:131]
	v_mov_b32_e32 v151, v170
	v_mov_b32_e32 v159, v171
	v_mov_b32_e32 v165, v172
	v_mov_b32_e32 v167, v173
	v_pk_add_f32 v[150:151], v[150:151], v[158:159]
	v_pk_add_f32 v[158:159], v[164:165], v[166:167]
	s_nop 0
	v_pk_add_f32 v[150:151], v[150:151], v[158:159]
	s_nop 0
	v_add_f32_e32 v150, v150, v151
	ds_bpermute_b32 v151, v61, v150
	s_waitcnt lgkmcnt(0)
	v_add_f32_e32 v150, v150, v151
	ds_bpermute_b32 v151, v73, v150
	s_waitcnt lgkmcnt(0)
	v_add_f32_e32 v150, v150, v151
	ds_bpermute_b32 v151, v74, v150
	s_waitcnt lgkmcnt(0)
	v_add_f32_e32 v150, v150, v151
	ds_bpermute_b32 v151, v75, v150
	s_waitcnt lgkmcnt(0)
	v_add_f32_e32 v150, v150, v151
	ds_bpermute_b32 v151, v76, v150
	s_waitcnt lgkmcnt(0)
	v_add_f32_e32 v34, v150, v151
	ds_bpermute_b32 v35, v109, v34
	v_mov_b32_e32 v109, 0
	s_waitcnt lgkmcnt(0)
	v_add_f32_e32 v34, v34, v35
	v_fmamk_f32 v34, v34, 0x3a000000, v67
	v_mul_f32_e32 v35, 0x4b800000, v34
	v_cmp_gt_f32_e32 vcc, s38, v34
	s_nop 1
	v_cndmask_b32_e32 v34, v34, v35, vcc
	v_rsq_f32_e32 v34, v34
	s_nop 0
	v_mul_f32_e32 v35, 0x45800000, v34
	v_cndmask_b32_e32 v34, v34, v35, vcc
	v_pk_mul_f32 v[36:37], v[34:35], v[146:147] op_sel_hi:[0,1]
	v_pk_mul_f32 v[36:37], v[30:31], v[36:37]
	v_pk_mul_f32 v[38:39], v[34:35], v[132:133] op_sel_hi:[0,1]
	v_mov_b32_e32 v35, 0
	v_cvt_pk_fp8_f32 v35, v36, v37
	v_pk_mul_f32 v[38:39], v[32:33], v[38:39]
	ds_write2_b64 v63, v[36:37], v[38:39] offset1:1
	v_pk_mul_f32 v[40:41], v[34:35], v[148:149] op_sel_hi:[0,1]
	v_cvt_pk_fp8_f32 v35, v38, v39 op_sel:[0,0,1]
	v_pk_mul_f32 v[40:41], v[26:27], v[40:41]
	v_pk_mul_f32 v[36:37], v[34:35], v[152:153] op_sel_hi:[0,1]
	v_pk_mul_f32 v[42:43], v[34:35], v[134:135] op_sel_hi:[0,1]
	global_store_dword v[44:45], v35, off
	v_pk_mul_f32 v[36:37], v[22:23], v[36:37]
	v_pk_mul_f32 v[38:39], v[34:35], v[136:137] op_sel_hi:[0,1]
	v_mov_b32_e32 v35, 0
	v_cvt_pk_fp8_f32 v35, v36, v37
	v_cvt_pk_fp8_f32 v109, v40, v41
	v_pk_mul_f32 v[42:43], v[28:29], v[42:43]
	v_pk_mul_f32 v[38:39], v[24:25], v[38:39]
	ds_write2_b64 v63, v[40:41], v[42:43] offset0:128 offset1:129
	v_pk_mul_f32 v[40:41], v[34:35], v[156:157] op_sel_hi:[0,1]
	v_cvt_pk_fp8_f32 v35, v38, v39 op_sel:[0,0,1]
	v_cvt_pk_fp8_f32 v109, v42, v43 op_sel:[0,0,1]
	v_pk_mul_f32 v[40:41], v[18:19], v[40:41]
	v_pk_mul_f32 v[42:43], v[34:35], v[138:139] op_sel_hi:[0,1]
	global_store_dword v[44:45], v35, off offset:512
	v_add_u32_e32 v35, 0x800, v63
	global_store_dword v[44:45], v109, off offset:256
	v_mov_b32_e32 v109, 0
	ds_write2_b64 v35, v[36:37], v[38:39] offset1:1
	v_add_u32_e32 v35, 0xc00, v63
	v_cvt_pk_fp8_f32 v109, v40, v41
	v_pk_mul_f32 v[42:43], v[20:21], v[42:43]
	v_pk_mul_f32 v[36:37], v[34:35], v[162:163] op_sel_hi:[0,1]
	ds_write2_b64 v35, v[40:41], v[42:43] offset1:1
	v_pk_mul_f32 v[36:37], v[14:15], v[36:37]
	v_pk_mul_f32 v[38:39], v[34:35], v[140:141] op_sel_hi:[0,1]
	v_mov_b32_e32 v35, 0
	v_cvt_pk_fp8_f32 v35, v36, v37
	v_cvt_pk_fp8_f32 v109, v42, v43 op_sel:[0,0,1]
	v_pk_mul_f32 v[38:39], v[16:17], v[38:39]
	v_pk_mul_f32 v[40:41], v[34:35], v[154:155] op_sel_hi:[0,1]
	v_cvt_pk_fp8_f32 v35, v38, v39 op_sel:[0,0,1]
	global_store_dword v[44:45], v109, off offset:768
	v_pk_mul_f32 v[40:41], v[10:11], v[40:41]
	v_mov_b32_e32 v109, 0
	v_cvt_pk_fp8_f32 v109, v40, v41
	v_pk_mul_f32 v[42:43], v[34:35], v[142:143] op_sel_hi:[0,1]
	global_store_dword v[44:45], v35, off offset:1024
	v_add_u32_e32 v35, 0x1000, v63
	ds_write2_b64 v35, v[36:37], v[38:39] offset1:1
	v_add_u32_e32 v35, 0x1400, v63
	v_pk_mul_f32 v[42:43], v[12:13], v[42:43]
	v_pk_mul_f32 v[36:37], v[34:35], v[160:161] op_sel_hi:[0,1]
	v_cvt_pk_fp8_f32 v109, v42, v43 op_sel:[0,0,1]
	ds_write2_b64 v35, v[40:41], v[42:43] offset1:1
	v_pk_mul_f32 v[36:37], v[6:7], v[36:37]
	v_mov_b32_e32 v42, 0
	v_cvt_pk_fp8_f32 v42, v36, v37
	v_pk_mul_f32 v[40:41], v[34:35], v[168:169] op_sel_hi:[0,1]
	v_pk_mul_f32 v[38:39], v[34:35], v[144:145] op_sel_hi:[0,1]
	v_pk_mul_f32 v[40:41], v[2:3], v[40:41]
	v_mov_b32_e32 v43, 0
	v_pk_mul_f32 v[38:39], v[8:9], v[38:39]
	v_cvt_pk_fp8_f32 v43, v40, v41
	v_cvt_pk_fp8_f32 v42, v38, v39 op_sel:[0,0,1]
	v_pk_mul_f32 v[34:35], v[34:35], v[130:131] op_sel_hi:[0,1]
	v_pk_mul_f32 v[34:35], v[4:5], v[34:35]
	global_store_dword v[44:45], v109, off offset:1280
	v_cvt_pk_fp8_f32 v43, v34, v35 op_sel:[0,0,1]
	global_store_dword v[44:45], v42, off offset:1536
	v_add_u32_e32 v42, 0x1800, v63
	ds_write2_b64 v42, v[36:37], v[38:39] offset1:1
	v_add_u32_e32 v36, 0x1c00, v63
	ds_write2_b64 v36, v[40:41], v[34:35] offset1:1
	v_mov_b64_e32 v[34:35], v[48:49]
	global_store_dword v[44:45], v43, off offset:1792
	s_waitcnt lgkmcnt(0)
	s_barrier
	global_load_dword v109, v[34:35], off
	global_load_dword v122, v[34:35], off offset:64
	global_load_dword v123, v[34:35], off offset:512
	global_load_dword v124, v[34:35], off offset:576
	global_load_dword v125, v[34:35], off offset:1024
	global_load_dword v126, v[34:35], off offset:1088
	global_load_dword v127, v[34:35], off offset:1536
	global_load_dword v128, v[34:35], off offset:1600
	global_load_dword v129, v[34:35], off offset:2048
	global_load_dword v130, v[34:35], off offset:2112
	global_load_dword v131, v[34:35], off offset:2560
	global_load_dword v132, v[34:35], off offset:2624
	global_load_dword v133, v[34:35], off offset:3072
	global_load_dword v134, v[34:35], off offset:3136
	global_load_dword v135, v[34:35], off offset:3584
	global_load_dword v136, v[34:35], off offset:3648
	v_add_co_u32_e32 v34, vcc, s33, v34
	s_nop 1
	v_addc_co_u32_e32 v35, vcc, 0, v35, vcc
	global_load_dword v137, v[34:35], off
	global_load_dword v138, v[34:35], off offset:64
	global_load_dword v139, v[34:35], off offset:512
	global_load_dword v140, v[34:35], off offset:576
	global_load_dword v141, v[34:35], off offset:1024
	global_load_dword v142, v[34:35], off offset:1088
	global_load_dword v143, v[34:35], off offset:1536
	global_load_dword v144, v[34:35], off offset:1600
	global_load_dword v145, v[34:35], off offset:2048
	global_load_dword v146, v[34:35], off offset:2112
	global_load_dword v147, v[34:35], off offset:2560
	global_load_dword v148, v[34:35], off offset:2624
	global_load_dword v149, v[34:35], off offset:3072
	global_load_dword v150, v[34:35], off offset:3136
	global_load_dword v151, v[34:35], off offset:3584
	global_load_dword v152, v[34:35], off offset:3648
	ds_read2_b32 v[42:43], v68 offset1:4
	ds_read2_b32 v[44:45], v68 offset0:8 offset1:12
	ds_read2_b32 v[110:111], v68 offset0:16 offset1:20
	ds_read2_b32 v[112:113], v68 offset0:24 offset1:28
	ds_read2_b32 v[114:115], v68 offset0:32 offset1:36
	ds_read2_b32 v[116:117], v68 offset0:40 offset1:44
	ds_read2_b32 v[118:119], v68 offset0:48 offset1:52
	ds_read2_b32 v[120:121], v68 offset0:56 offset1:60
	s_waitcnt lgkmcnt(7)
	v_mfma_f32_16x16x4_f32 v[34:37], v42, v93, 0
	v_mfma_f32_16x16x4_f32 v[34:37], v43, v94, v[34:37]
	s_waitcnt lgkmcnt(6)
	v_mfma_f32_16x16x4_f32 v[34:37], v44, v95, v[34:37]
	v_mfma_f32_16x16x4_f32 v[38:41], v42, v81, 0
	v_mfma_f32_16x16x4_f32 v[34:37], v45, v96, v[34:37]
	v_mfma_f32_16x16x4_f32 v[38:41], v43, v82, v[38:41]
	v_mov_b64_e32 v[42:43], v[50:51]
	s_waitcnt lgkmcnt(5)
	v_mfma_f32_16x16x4_f32 v[34:37], v110, v97, v[34:37]
	v_mfma_f32_16x16x4_f32 v[38:41], v44, v83, v[38:41]
	v_mfma_f32_16x16x4_f32 v[34:37], v111, v98, v[34:37]
	v_mfma_f32_16x16x4_f32 v[38:41], v45, v84, v[38:41]
	s_waitcnt lgkmcnt(4)
	v_mfma_f32_16x16x4_f32 v[34:37], v112, v99, v[34:37]
	v_mfma_f32_16x16x4_f32 v[38:41], v110, v85, v[38:41]
	v_mfma_f32_16x16x4_f32 v[34:37], v113, v100, v[34:37]
	v_mfma_f32_16x16x4_f32 v[38:41], v111, v87, v[38:41]
	s_waitcnt lgkmcnt(3)
	v_mfma_f32_16x16x4_f32 v[34:37], v114, v101, v[34:37]
	v_mfma_f32_16x16x4_f32 v[38:41], v112, v88, v[38:41]
	v_mfma_f32_16x16x4_f32 v[34:37], v115, v102, v[34:37]
	v_mfma_f32_16x16x4_f32 v[38:41], v113, v89, v[38:41]
	s_waitcnt lgkmcnt(2)
	v_mfma_f32_16x16x4_f32 v[34:37], v116, v103, v[34:37]
	v_mfma_f32_16x16x4_f32 v[38:41], v114, v91, v[38:41]
	v_mfma_f32_16x16x4_f32 v[34:37], v117, v104, v[34:37]
	v_mfma_f32_16x16x4_f32 v[38:41], v115, v92, v[38:41]
	global_load_dword v92, v[42:43], off
	global_load_dword v93, v[42:43], off offset:64
	global_load_dword v94, v[42:43], off offset:512
	global_load_dword v95, v[42:43], off offset:576
	global_load_dword v96, v[42:43], off offset:1024
	global_load_dword v97, v[42:43], off offset:1088
	global_load_dword v98, v[42:43], off offset:1536
	global_load_dword v99, v[42:43], off offset:1600
	s_waitcnt lgkmcnt(1)
	v_mfma_f32_16x16x4_f32 v[34:37], v118, v105, v[34:37]
	v_mfma_f32_16x16x4_f32 v[38:41], v116, v90, v[38:41]
	v_mfma_f32_16x16x4_f32 v[34:37], v119, v106, v[34:37]
	v_mfma_f32_16x16x4_f32 v[38:41], v117, v86, v[38:41]
	s_waitcnt lgkmcnt(0)
	v_mfma_f32_16x16x4_f32 v[34:37], v120, v107, v[34:37]
	global_load_dword v100, v[42:43], off offset:2048
	global_load_dword v101, v[42:43], off offset:2112
	global_load_dword v102, v[42:43], off offset:2560
	global_load_dword v103, v[42:43], off offset:2624
	global_load_dword v104, v[42:43], off offset:3072
	global_load_dword v105, v[42:43], off offset:3136
	global_load_dword v106, v[42:43], off offset:3584
	global_load_dword v107, v[42:43], off offset:3648
	v_add_co_u32_e32 v42, vcc, s33, v42
	s_nop 1
	v_addc_co_u32_e32 v43, vcc, 0, v43, vcc
	v_mfma_f32_16x16x4_f32 v[38:41], v118, v80, v[38:41]
	v_mfma_f32_16x16x4_f32 v[34:37], v121, v108, v[34:37]
	global_load_dword v108, v[42:43], off
	global_load_dword v110, v[42:43], off offset:64
	global_load_dword v111, v[42:43], off offset:512
	global_load_dword v112, v[42:43], off offset:576
	global_load_dword v113, v[42:43], off offset:1024
	global_load_dword v114, v[42:43], off offset:1088
	global_load_dword v115, v[42:43], off offset:1536
	global_load_dword v116, v[42:43], off offset:1600
	v_mfma_f32_16x16x4_f32 v[38:41], v119, v79, v[38:41]
	global_load_dword v117, v[42:43], off offset:2048
	global_load_dword v118, v[42:43], off offset:2112
	global_load_dword v119, v[42:43], off offset:2560
	global_load_dword v153, v[42:43], off offset:2624
	global_load_dword v154, v[42:43], off offset:3072
	global_load_dword v155, v[42:43], off offset:3136
	global_load_dword v156, v[42:43], off offset:3584
	global_load_dword v157, v[42:43], off offset:3648
	ds_read2_b32 v[42:43], v1 offset0:64 offset1:68
	v_mfma_f32_16x16x4_f32 v[38:41], v120, v78, v[38:41]
	ds_read2_b32 v[44:45], v1 offset0:72 offset1:76
	ds_read2_b32 v[78:79], v1 offset0:80 offset1:84
	ds_read2_b32 v[80:81], v1 offset0:88 offset1:92
	ds_read2_b32 v[82:83], v1 offset0:96 offset1:100
	ds_read2_b32 v[84:85], v1 offset0:104 offset1:108
	ds_read2_b32 v[86:87], v1 offset0:112 offset1:116
	ds_read2_b32 v[88:89], v1 offset0:120 offset1:124
	v_mfma_f32_16x16x4_f32 v[38:41], v121, v77, v[38:41]
	s_waitcnt vmcnt(62) lgkmcnt(7)
	v_mfma_f32_16x16x4_f32 v[34:37], v42, v109, v[34:37]
	s_waitcnt vmcnt(61)
	v_mfma_f32_16x16x4_f32 v[34:37], v43, v123, v[34:37]
	v_mfma_f32_16x16x4_f32 v[38:41], v42, v122, v[38:41]
	s_waitcnt vmcnt(59) lgkmcnt(6)
	v_mfma_f32_16x16x4_f32 v[34:37], v44, v125, v[34:37]
	v_mfma_f32_16x16x4_f32 v[38:41], v43, v124, v[38:41]
	v_mov_b64_e32 v[42:43], v[52:53]
	global_load_dword v77, v[42:43], off
	global_load_dword v109, v[42:43], off offset:64
	global_load_dword v120, v[42:43], off offset:512
	global_load_dword v121, v[42:43], off offset:576
	global_load_dword v122, v[42:43], off offset:1024
	global_load_dword v123, v[42:43], off offset:1088
	global_load_dword v124, v[42:43], off offset:1536
	global_load_dword v125, v[42:43], off offset:1600
	s_waitcnt vmcnt(62)
	v_mfma_f32_16x16x4_f32 v[34:37], v45, v127, v[34:37]
	v_mfma_f32_16x16x4_f32 v[38:41], v44, v126, v[38:41]
	s_waitcnt lgkmcnt(5)
	v_mfma_f32_16x16x4_f32 v[34:37], v78, v129, v[34:37]
	v_mfma_f32_16x16x4_f32 v[38:41], v45, v128, v[38:41]
	s_waitcnt vmcnt(61)
	v_mfma_f32_16x16x4_f32 v[34:37], v79, v131, v[34:37]
	v_mfma_f32_16x16x4_f32 v[38:41], v78, v130, v[38:41]
	s_waitcnt vmcnt(59) lgkmcnt(4)
	v_mfma_f32_16x16x4_f32 v[34:37], v80, v133, v[34:37]
	v_mfma_f32_16x16x4_f32 v[38:41], v79, v132, v[38:41]
	global_load_dword v126, v[42:43], off offset:2048
	global_load_dword v127, v[42:43], off offset:2112
	global_load_dword v128, v[42:43], off offset:2560
	global_load_dword v129, v[42:43], off offset:2624
	global_load_dword v130, v[42:43], off offset:3072
	global_load_dword v131, v[42:43], off offset:3136
	global_load_dword v132, v[42:43], off offset:3584
	global_load_dword v133, v[42:43], off offset:3648
	v_add_co_u32_e32 v42, vcc, s33, v42
	s_nop 1
	v_addc_co_u32_e32 v43, vcc, 0, v43, vcc
	s_waitcnt vmcnt(62)
	v_mfma_f32_16x16x4_f32 v[34:37], v81, v135, v[34:37]
	v_mfma_f32_16x16x4_f32 v[38:41], v80, v134, v[38:41]
	s_waitcnt lgkmcnt(3)
	v_mfma_f32_16x16x4_f32 v[34:37], v82, v137, v[34:37]
	v_mfma_f32_16x16x4_f32 v[38:41], v81, v136, v[38:41]
	s_waitcnt vmcnt(61)
	v_mfma_f32_16x16x4_f32 v[34:37], v83, v139, v[34:37]
	v_mfma_f32_16x16x4_f32 v[38:41], v82, v138, v[38:41]
	s_waitcnt vmcnt(59) lgkmcnt(2)
	v_mfma_f32_16x16x4_f32 v[34:37], v84, v141, v[34:37]
	v_mfma_f32_16x16x4_f32 v[38:41], v83, v140, v[38:41]
	global_load_dword v134, v[42:43], off
	global_load_dword v135, v[42:43], off offset:64
	global_load_dword v136, v[42:43], off offset:512
	global_load_dword v137, v[42:43], off offset:576
	global_load_dword v138, v[42:43], off offset:1024
	global_load_dword v139, v[42:43], off offset:1088
	global_load_dword v140, v[42:43], off offset:1536
	global_load_dword v141, v[42:43], off offset:1600
	s_waitcnt vmcnt(62)
	v_mfma_f32_16x16x4_f32 v[34:37], v85, v143, v[34:37]
	v_mfma_f32_16x16x4_f32 v[38:41], v84, v142, v[38:41]
	s_waitcnt lgkmcnt(1)
	v_mfma_f32_16x16x4_f32 v[34:37], v86, v145, v[34:37]
	v_mfma_f32_16x16x4_f32 v[38:41], v85, v144, v[38:41]
	s_waitcnt vmcnt(61)
	v_mfma_f32_16x16x4_f32 v[34:37], v87, v147, v[34:37]
	v_mfma_f32_16x16x4_f32 v[38:41], v86, v146, v[38:41]
	s_waitcnt vmcnt(59) lgkmcnt(0)
	v_mfma_f32_16x16x4_f32 v[34:37], v88, v149, v[34:37]
	v_mfma_f32_16x16x4_f32 v[38:41], v87, v148, v[38:41]
	global_load_dword v142, v[42:43], off offset:2048
	global_load_dword v143, v[42:43], off offset:2112
	global_load_dword v144, v[42:43], off offset:2560
	global_load_dword v145, v[42:43], off offset:2624
	global_load_dword v146, v[42:43], off offset:3072
	global_load_dword v147, v[42:43], off offset:3136
	global_load_dword v148, v[42:43], off offset:3584
	global_load_dword v149, v[42:43], off offset:3648
	ds_read2_b32 v[42:43], v1 offset0:128 offset1:132
	ds_read2_b32 v[44:45], v1 offset0:136 offset1:140
	ds_read2_b32 v[78:79], v1 offset0:144 offset1:148
	ds_read2_b32 v[80:81], v1 offset0:152 offset1:156
	ds_read2_b32 v[82:83], v1 offset0:160 offset1:164
	ds_read2_b32 v[84:85], v1 offset0:168 offset1:172
	ds_read2_b32 v[86:87], v1 offset0:176 offset1:180
	ds_read2_b32 v[90:91], v1 offset0:184 offset1:188
	s_waitcnt vmcnt(62)
	v_mfma_f32_16x16x4_f32 v[34:37], v89, v151, v[34:37]
	v_mfma_f32_16x16x4_f32 v[38:41], v88, v150, v[38:41]
	v_mfma_f32_16x16x4_f32 v[38:41], v89, v152, v[38:41]
	s_waitcnt lgkmcnt(7)
	v_mfma_f32_16x16x4_f32 v[34:37], v42, v92, v[34:37]
	v_mfma_f32_16x16x4_f32 v[38:41], v42, v93, v[38:41]
	s_waitcnt vmcnt(61)
	v_mfma_f32_16x16x4_f32 v[34:37], v43, v94, v[34:37]
	s_waitcnt vmcnt(60)
	v_mfma_f32_16x16x4_f32 v[38:41], v43, v95, v[38:41]
	ds_read2_b32 v[42:43], v1 offset0:192 offset1:196
	s_waitcnt vmcnt(59) lgkmcnt(7)
	v_mfma_f32_16x16x4_f32 v[34:37], v44, v96, v[34:37]
	s_waitcnt vmcnt(58)
	v_mfma_f32_16x16x4_f32 v[38:41], v44, v97, v[38:41]
	s_waitcnt vmcnt(57)
	v_mfma_f32_16x16x4_f32 v[34:37], v45, v98, v[34:37]
	s_waitcnt vmcnt(56)
	v_mfma_f32_16x16x4_f32 v[38:41], v45, v99, v[38:41]
	s_waitcnt vmcnt(55) lgkmcnt(6)
	v_mfma_f32_16x16x4_f32 v[34:37], v78, v100, v[34:37]
	s_waitcnt vmcnt(54)
	v_mfma_f32_16x16x4_f32 v[38:41], v78, v101, v[38:41]
	s_waitcnt vmcnt(53)
	v_mfma_f32_16x16x4_f32 v[34:37], v79, v102, v[34:37]
	s_waitcnt vmcnt(52)
	v_mfma_f32_16x16x4_f32 v[38:41], v79, v103, v[38:41]
	s_waitcnt vmcnt(51) lgkmcnt(5)
	v_mfma_f32_16x16x4_f32 v[34:37], v80, v104, v[34:37]
	s_waitcnt vmcnt(50)
	v_mfma_f32_16x16x4_f32 v[38:41], v80, v105, v[38:41]
	s_waitcnt vmcnt(49)
	v_mfma_f32_16x16x4_f32 v[34:37], v81, v106, v[34:37]
	s_waitcnt vmcnt(48)
	v_mfma_f32_16x16x4_f32 v[38:41], v81, v107, v[38:41]
	s_waitcnt vmcnt(47) lgkmcnt(4)
	v_mfma_f32_16x16x4_f32 v[34:37], v82, v108, v[34:37]
	s_waitcnt vmcnt(46)
	v_mfma_f32_16x16x4_f32 v[38:41], v82, v110, v[38:41]
	s_waitcnt vmcnt(45)
	v_mfma_f32_16x16x4_f32 v[34:37], v83, v111, v[34:37]
	s_waitcnt vmcnt(44)
	v_mfma_f32_16x16x4_f32 v[38:41], v83, v112, v[38:41]
	s_waitcnt vmcnt(43) lgkmcnt(3)
	v_mfma_f32_16x16x4_f32 v[34:37], v84, v113, v[34:37]
	s_waitcnt vmcnt(42)
	v_mfma_f32_16x16x4_f32 v[38:41], v84, v114, v[38:41]
	s_waitcnt vmcnt(41)
	v_mfma_f32_16x16x4_f32 v[34:37], v85, v115, v[34:37]
	s_waitcnt vmcnt(40)
	v_mfma_f32_16x16x4_f32 v[38:41], v85, v116, v[38:41]
	s_waitcnt vmcnt(39) lgkmcnt(2)
	v_mfma_f32_16x16x4_f32 v[34:37], v86, v117, v[34:37]
	s_waitcnt vmcnt(38)
	v_mfma_f32_16x16x4_f32 v[38:41], v86, v118, v[38:41]
	s_waitcnt vmcnt(37)
	v_mfma_f32_16x16x4_f32 v[34:37], v87, v119, v[34:37]
	s_waitcnt vmcnt(36)
	v_mfma_f32_16x16x4_f32 v[38:41], v87, v153, v[38:41]
	ds_read2_b32 v[44:45], v1 offset0:200 offset1:204
	ds_read2_b32 v[78:79], v1 offset0:208 offset1:212
	ds_read2_b32 v[80:81], v1 offset0:216 offset1:220
	ds_read2_b32 v[82:83], v1 offset0:224 offset1:228
	ds_read2_b32 v[84:85], v1 offset0:232 offset1:236
	ds_read2_b32 v[86:87], v1 offset0:240 offset1:244
	ds_read2_b32 v[88:89], v1 offset0:248 offset1:252
	s_waitcnt vmcnt(35) lgkmcnt(8)
	v_mfma_f32_16x16x4_f32 v[34:37], v90, v154, v[34:37]
	s_waitcnt vmcnt(34)
	v_mfma_f32_16x16x4_f32 v[38:41], v90, v155, v[38:41]
	s_waitcnt vmcnt(33)
	v_mfma_f32_16x16x4_f32 v[34:37], v91, v156, v[34:37]
	s_waitcnt vmcnt(32)
	v_mfma_f32_16x16x4_f32 v[38:41], v91, v157, v[38:41]
	s_waitcnt vmcnt(31) lgkmcnt(7)
	v_mfma_f32_16x16x4_f32 v[34:37], v42, v77, v[34:37]
	s_waitcnt lgkmcnt(0)
	s_barrier
	s_mov_b64 s[12:13], -1
	s_mov_b64 s[10:11], -1
	s_waitcnt vmcnt(30)
	v_mfma_f32_16x16x4_f32 v[38:41], v42, v109, v[38:41]
	s_waitcnt vmcnt(29)
	v_mfma_f32_16x16x4_f32 v[34:37], v43, v120, v[34:37]
	s_waitcnt vmcnt(28)
	v_mfma_f32_16x16x4_f32 v[38:41], v43, v121, v[38:41]
	s_waitcnt vmcnt(27)
	v_mfma_f32_16x16x4_f32 v[34:37], v44, v122, v[34:37]
	s_waitcnt vmcnt(26)
	v_mfma_f32_16x16x4_f32 v[38:41], v44, v123, v[38:41]
	s_waitcnt vmcnt(25)
	v_mfma_f32_16x16x4_f32 v[34:37], v45, v124, v[34:37]
	s_waitcnt vmcnt(24)
	v_mfma_f32_16x16x4_f32 v[38:41], v45, v125, v[38:41]
	s_waitcnt vmcnt(23)
	v_mfma_f32_16x16x4_f32 v[34:37], v78, v126, v[34:37]
	s_waitcnt vmcnt(22)
	v_mfma_f32_16x16x4_f32 v[38:41], v78, v127, v[38:41]
	s_waitcnt vmcnt(21)
	v_mfma_f32_16x16x4_f32 v[34:37], v79, v128, v[34:37]
	s_waitcnt vmcnt(20)
	v_mfma_f32_16x16x4_f32 v[38:41], v79, v129, v[38:41]
	s_waitcnt vmcnt(19)
	v_mfma_f32_16x16x4_f32 v[34:37], v80, v130, v[34:37]
	s_waitcnt vmcnt(18)
	v_mfma_f32_16x16x4_f32 v[38:41], v80, v131, v[38:41]
	s_waitcnt vmcnt(17)
	v_mfma_f32_16x16x4_f32 v[34:37], v81, v132, v[34:37]
	s_waitcnt vmcnt(16)
	v_mfma_f32_16x16x4_f32 v[38:41], v81, v133, v[38:41]
	s_waitcnt vmcnt(15)
	v_mfma_f32_16x16x4_f32 v[34:37], v82, v134, v[34:37]
	s_waitcnt vmcnt(14)
	v_mfma_f32_16x16x4_f32 v[38:41], v82, v135, v[38:41]
	s_waitcnt vmcnt(13)
	v_mfma_f32_16x16x4_f32 v[34:37], v83, v136, v[34:37]
	s_waitcnt vmcnt(12)
	v_mfma_f32_16x16x4_f32 v[38:41], v83, v137, v[38:41]
	s_waitcnt vmcnt(11)
	v_mfma_f32_16x16x4_f32 v[34:37], v84, v138, v[34:37]
	s_waitcnt vmcnt(10)
	v_mfma_f32_16x16x4_f32 v[38:41], v84, v139, v[38:41]
	s_waitcnt vmcnt(9)
	v_mfma_f32_16x16x4_f32 v[34:37], v85, v140, v[34:37]
	s_waitcnt vmcnt(8)
	v_mfma_f32_16x16x4_f32 v[38:41], v85, v141, v[38:41]
	s_waitcnt vmcnt(7)
	v_mfma_f32_16x16x4_f32 v[34:37], v86, v142, v[34:37]
	s_waitcnt vmcnt(6)
	v_mfma_f32_16x16x4_f32 v[38:41], v86, v143, v[38:41]
	s_waitcnt vmcnt(5)
	v_mfma_f32_16x16x4_f32 v[34:37], v87, v144, v[34:37]
	s_waitcnt vmcnt(4)
	v_mfma_f32_16x16x4_f32 v[38:41], v87, v145, v[38:41]
	s_waitcnt vmcnt(3)
	v_mfma_f32_16x16x4_f32 v[34:37], v88, v146, v[34:37]
	s_waitcnt vmcnt(2)
	v_mfma_f32_16x16x4_f32 v[38:41], v88, v147, v[38:41]
	s_waitcnt vmcnt(1)
	v_mfma_f32_16x16x4_f32 v[34:37], v89, v148, v[34:37]
	s_waitcnt vmcnt(0)
	v_mfma_f32_16x16x4_f32 v[38:41], v89, v149, v[38:41]
	s_nop 9
	ds_write2_b32 v69, v34, v38 offset1:16
	ds_write2_b32 v69, v35, v39 offset0:32 offset1:48
	ds_write2_b32 v69, v36, v40 offset0:64 offset1:80
	ds_write2_b32 v69, v37, v41 offset0:96 offset1:112
	s_waitcnt lgkmcnt(0)
	s_barrier
	global_load_dword v38, v[54:55], off
	ds_read2st64_b32 v[34:35], v65 offset1:8
	ds_read2st64_b32 v[36:37], v65 offset0:16 offset1:24
	s_waitcnt vmcnt(0) lgkmcnt(1)
	v_add_f32_e32 v34, v38, v34
	ds_read2st64_b32 v[38:39], v65 offset0:32 offset1:40
	v_add_f32_e32 v40, v34, v35
	ds_read2st64_b32 v[34:35], v65 offset0:48 offset1:56
	s_waitcnt lgkmcnt(2)
	v_add_f32_e32 v36, v40, v36
	v_add_f32_e32 v36, v36, v37
	s_waitcnt lgkmcnt(1)
	v_add_f32_e32 v36, v36, v38
	v_add_f32_e32 v36, v36, v39
	s_waitcnt lgkmcnt(0)
	v_add_f32_e32 v34, v36, v34
	v_add_f32_e32 v37, v34, v35
	ds_bpermute_b32 v34, v76, v37
	ds_bpermute_b32 v35, v76, v64
	s_waitcnt lgkmcnt(1)
	v_cmp_nlt_f32_e32 vcc, v37, v34
	s_and_saveexec_b64 s[24:25], vcc
	s_cbranch_execz .LBB0_828
	v_cmp_eq_f32_e32 vcc, v37, v34
	s_waitcnt lgkmcnt(0)
	v_cmp_lt_i32_e64 s[10:11], v35, v64
	s_and_b64 s[10:11], vcc, s[10:11]
	s_orn2_b64 s[10:11], s[10:11], exec
